# adds P7 router-constant sums: 32 loads in flight per sum instead of 4 drained groups of 8
# baseline (speedup 1.0000x reference)
; __device__ __forceinline__ void p7_router(Frame& F, const Args& A, bool commit = true) {
;     ...
;         { const int token = F.tid & 31, eg = F.tid >> 5; float s2 = 0.f;
; #pragma unroll
;           for (int w = 0; w < 8; ++w) s2 += ssp[w * 64 + token] + ssp[w * 64 + 32 + token];
;           const float rstd = 1.0f / sqrtf(s2 * (1.0f / DM) + EPS);
; #pragma unroll
;           for (int q = 0; q < 2; ++q) { const int e = eg * 2 + q; float raw = 0.f;
; #pragma unroll
;               for (int w = 0; w < 8; ++w) raw += part[(w * 32 + token) * 32 + e];
;               float rc = A.in[I_BR][e];
; #pragma unroll 8
;               for (int kq = 0; kq < 32; ++kq) rc += RC[(bb * 32 + kq) * 32 + e];
;               logitL[token * 33 + e] = rstd * raw + rc; }
.LBB0_897:
	v_mov_b32_e32 v28, v27
	v_ashrrev_i32_e32 v29, 31, v27
	v_lshl_add_u64 v[28:29], v[28:29], 2, s[14:15]
	global_load_dword v230, v[28:29], off
	global_load_dword v231, v[28:29], off offset:128
	global_load_dword v232, v[28:29], off offset:256
	global_load_dword v233, v[28:29], off offset:384
	global_load_dword v234, v[28:29], off offset:512
	global_load_dword v235, v[28:29], off offset:640
	global_load_dword v236, v[28:29], off offset:768
	global_load_dword v237, v[28:29], off offset:896
	global_load_dword v238, v[28:29], off offset:1024
	global_load_dword v239, v[28:29], off offset:1152
	global_load_dword v240, v[28:29], off offset:1280
	global_load_dword v241, v[28:29], off offset:1408
	global_load_dword v242, v[28:29], off offset:1536
	global_load_dword v243, v[28:29], off offset:1664
	global_load_dword v244, v[28:29], off offset:1792
	global_load_dword v245, v[28:29], off offset:1920
	global_load_dword v248, v[28:29], off offset:2048
	global_load_dword v249, v[28:29], off offset:2176
	global_load_dword v250, v[28:29], off offset:2304
	global_load_dword v251, v[28:29], off offset:2432
	global_load_dword v252, v[28:29], off offset:2560
	global_load_dword v253, v[28:29], off offset:2688
	global_load_dword v254, v[28:29], off offset:2816
	global_load_dword v255, v[28:29], off offset:2944
	global_load_dword v200, v[28:29], off offset:3072
	global_load_dword v201, v[28:29], off offset:3200
	global_load_dword v202, v[28:29], off offset:3328
	global_load_dword v204, v[28:29], off offset:3456
	global_load_dword v205, v[28:29], off offset:3584
	global_load_dword v109, v[28:29], off offset:3712
	global_load_dword v119, v[28:29], off offset:3840
	global_load_dword v189, v[28:29], off offset:3968
	s_waitcnt vmcnt(31)
	v_add_f32_e32 v26, v26, v230
	s_waitcnt vmcnt(30)
	v_add_f32_e32 v26, v26, v231
	s_waitcnt vmcnt(29)
	v_add_f32_e32 v26, v26, v232
	s_waitcnt vmcnt(28)
	v_add_f32_e32 v26, v26, v233
	s_waitcnt vmcnt(27)
	v_add_f32_e32 v26, v26, v234
	s_waitcnt vmcnt(26)
	v_add_f32_e32 v26, v26, v235
	s_waitcnt vmcnt(25)
	v_add_f32_e32 v26, v26, v236
	s_waitcnt vmcnt(24)
	v_add_f32_e32 v26, v26, v237
	s_waitcnt vmcnt(23)
	v_add_f32_e32 v26, v26, v238
	s_waitcnt vmcnt(22)
	v_add_f32_e32 v26, v26, v239
	s_waitcnt vmcnt(21)
	v_add_f32_e32 v26, v26, v240
	s_waitcnt vmcnt(20)
	v_add_f32_e32 v26, v26, v241
	s_waitcnt vmcnt(19)
	v_add_f32_e32 v26, v26, v242
	s_waitcnt vmcnt(18)
	v_add_f32_e32 v26, v26, v243
	s_waitcnt vmcnt(17)
	v_add_f32_e32 v26, v26, v244
	s_waitcnt vmcnt(16)
	v_add_f32_e32 v26, v26, v245
	s_waitcnt vmcnt(15)
	v_add_f32_e32 v26, v26, v248
	s_waitcnt vmcnt(14)
	v_add_f32_e32 v26, v26, v249
	s_waitcnt vmcnt(13)
	v_add_f32_e32 v26, v26, v250
	s_waitcnt vmcnt(12)
	v_add_f32_e32 v26, v26, v251
	s_waitcnt vmcnt(11)
	v_add_f32_e32 v26, v26, v252
	s_waitcnt vmcnt(10)
	v_add_f32_e32 v26, v26, v253
	s_waitcnt vmcnt(9)
	v_add_f32_e32 v26, v26, v254
	s_waitcnt vmcnt(8)
	v_add_f32_e32 v26, v26, v255
	s_waitcnt vmcnt(7)
	v_add_f32_e32 v26, v26, v200
	s_waitcnt vmcnt(6)
	v_add_f32_e32 v26, v26, v201
	s_waitcnt vmcnt(5)
	v_add_f32_e32 v26, v26, v202
	s_waitcnt vmcnt(4)
	v_add_f32_e32 v26, v26, v204
	s_waitcnt vmcnt(3)
	v_add_f32_e32 v26, v26, v205
	s_waitcnt vmcnt(2)
	v_add_f32_e32 v26, v26, v109
	s_waitcnt vmcnt(1)
	v_add_f32_e32 v26, v26, v119
	s_waitcnt vmcnt(0)
	v_add_f32_e32 v26, v26, v189
	global_load_dword v27, v[74:75], off
	s_waitcnt lgkmcnt(11)
	v_add_f32_e32 v24, v24, v25
	v_add_f32_e32 v24, 0, v24
	s_waitcnt lgkmcnt(10)
	v_add_f32_e32 v22, v22, v23
	v_add_f32_e32 v22, v24, v22
	s_waitcnt lgkmcnt(9)
	v_add_f32_e32 v20, v20, v21
	v_add_f32_e32 v20, v22, v20
	s_waitcnt lgkmcnt(8)
	v_add_f32_e32 v16, v16, v17
	v_add_f32_e32 v16, v20, v16
	s_waitcnt lgkmcnt(7)
	v_add_f32_e32 v17, v18, v19
	v_add_f32_e32 v16, v16, v17
	s_waitcnt lgkmcnt(6)
	v_add_f32_e32 v14, v14, v15
	v_add_f32_e32 v14, v16, v14
	s_waitcnt lgkmcnt(5)
	v_add_f32_e32 v12, v12, v13
	v_add_f32_e32 v12, v14, v12
	s_waitcnt lgkmcnt(4)
	v_add_f32_e32 v10, v10, v11
	v_add_f32_e32 v10, v12, v10
	v_fmamk_f32 v10, v10, 0x3a000000, v104
	v_mul_f32_e32 v11, 0x4f800000, v10
	v_cmp_gt_f32_e32 vcc, s34, v10
	s_waitcnt lgkmcnt(3)
	v_add_f32_e32 v8, 0, v8
	v_add_f32_e32 v8, v8, v9
	v_cndmask_b32_e32 v10, v10, v11, vcc
	v_sqrt_f32_e32 v11, v10
	s_waitcnt lgkmcnt(2)
	v_add_f32_e32 v6, v8, v6
	v_add_f32_e32 v6, v6, v7
	s_waitcnt lgkmcnt(1)
	v_add_f32_e32 v4, v6, v4
	v_add_u32_e32 v12, -1, v11
	v_fma_f32 v13, -v12, v11, v10
	v_cmp_ge_f32_e64 s[6:7], 0, v13
	v_add_u32_e32 v13, 1, v11
	v_add_f32_e32 v4, v4, v5
	v_cndmask_b32_e64 v12, v11, v12, s[6:7]
	v_fma_f32 v11, -v13, v11, v10
	v_cmp_lt_f32_e64 s[6:7], 0, v11
	s_waitcnt lgkmcnt(0)
	v_add_f32_e32 v2, v4, v2
	v_cndmask_b32_e64 v11, v12, v13, s[6:7]
	v_mul_f32_e32 v12, 0x37800000, v11
	v_cndmask_b32_e32 v11, v11, v12, vcc
	v_cmp_class_f32_e32 vcc, v10, v105
	s_nop 1
	v_cndmask_b32_e32 v10, v11, v10, vcc
	v_div_scale_f32 v11, s[6:7], v10, v10, 1.0
	v_rcp_f32_e32 v12, v11
	s_mov_b32 s6, 0
	v_fma_f32 v13, -v11, v12, 1.0
	v_fmac_f32_e32 v12, v13, v12
	v_div_scale_f32 v13, vcc, 1.0, v10, 1.0
	v_mul_f32_e32 v14, v13, v12
	v_fma_f32 v15, -v11, v14, v13
	v_fmac_f32_e32 v14, v15, v12
	v_fma_f32 v11, -v11, v14, v13
	v_div_fmas_f32 v11, v11, v12, v14
	v_div_fixup_f32 v10, v11, v10, 1.0
	v_add_f32_e32 v11, v2, v3
	ds_read2st64_b32 v[8:9], v97 offset0:64 offset1:80
	ds_read2st64_b32 v[6:7], v97 offset0:96 offset1:112
	ds_read2st64_b32 v[4:5], v97 offset0:128 offset1:144
	ds_read2st64_b32 v[2:3], v97 offset0:160 offset1:176
	v_fmac_f32_e32 v26, v10, v11
	v_add_u32_e32 v11, s44, v96
	ds_write_b32 v95, v26 offset:51200
; __device__ __forceinline__ void p7_router(Frame& F, const Args& A, bool commit = true) {
;     ...
;           for (int q = 0; q < 2; ++q) { const int e = eg * 2 + q; float raw = 0.f;
; #pragma unroll
;               for (int w = 0; w < 8; ++w) raw += part[(w * 32 + token) * 32 + e];
;               float rc = A.in[I_BR][e];
; #pragma unroll 8
;               for (int kq = 0; kq < 32; ++kq) rc += RC[(bb * 32 + kq) * 32 + e];
;               logitL[token * 33 + e] = rstd * raw + rc; }
;           if (eg == 0) rstdL[token] = rstd; }
;         __syncthreads();
;         int se[4] = {0, 0, 0, 0}, lp[4] = {0, 0, 0, 0}; float pv[4] = {0.f, 0.f, 0.f, 0.f};
;         if (F.tid < 32) {
;             float sv[4];
; #pragma unroll
;             for (int k = 0; k < 4; ++k) { float best = -INFINITY; int bi = 0;
;                 for (int e = 0; e < 32; ++e) { const float v = logitL[F.tid * 33 + e]; if (v > best) { best = v; bi = e; } }
;                 sv[k] = best; se[k] = bi; logitL[F.tid * 33 + bi] = -INFINITY; }
.LBB0_899:
	v_mov_b32_e32 v12, v11
	v_ashrrev_i32_e32 v13, 31, v11
	v_lshl_add_u64 v[12:13], v[12:13], 2, s[14:15]
	global_load_dword v230, v[12:13], off
	global_load_dword v231, v[12:13], off offset:128
	global_load_dword v232, v[12:13], off offset:256
	global_load_dword v233, v[12:13], off offset:384
	global_load_dword v234, v[12:13], off offset:512
	global_load_dword v235, v[12:13], off offset:640
	global_load_dword v236, v[12:13], off offset:768
	global_load_dword v237, v[12:13], off offset:896
	global_load_dword v238, v[12:13], off offset:1024
	global_load_dword v239, v[12:13], off offset:1152
	global_load_dword v240, v[12:13], off offset:1280
	global_load_dword v241, v[12:13], off offset:1408
	global_load_dword v242, v[12:13], off offset:1536
	global_load_dword v243, v[12:13], off offset:1664
	global_load_dword v244, v[12:13], off offset:1792
	global_load_dword v245, v[12:13], off offset:1920
	global_load_dword v248, v[12:13], off offset:2048
	global_load_dword v249, v[12:13], off offset:2176
	global_load_dword v250, v[12:13], off offset:2304
	global_load_dword v251, v[12:13], off offset:2432
	global_load_dword v252, v[12:13], off offset:2560
	global_load_dword v253, v[12:13], off offset:2688
	global_load_dword v254, v[12:13], off offset:2816
	global_load_dword v255, v[12:13], off offset:2944
	global_load_dword v200, v[12:13], off offset:3072
	global_load_dword v201, v[12:13], off offset:3200
	global_load_dword v202, v[12:13], off offset:3328
	global_load_dword v204, v[12:13], off offset:3456
	global_load_dword v205, v[12:13], off offset:3584
	global_load_dword v109, v[12:13], off offset:3712
	global_load_dword v119, v[12:13], off offset:3840
	global_load_dword v189, v[12:13], off offset:3968
	s_waitcnt vmcnt(31)
	v_add_f32_e32 v27, v27, v230
	s_waitcnt vmcnt(30)
	v_add_f32_e32 v27, v27, v231
	s_waitcnt vmcnt(29)
	v_add_f32_e32 v27, v27, v232
	s_waitcnt vmcnt(28)
	v_add_f32_e32 v27, v27, v233
	s_waitcnt vmcnt(27)
	v_add_f32_e32 v27, v27, v234
	s_waitcnt vmcnt(26)
	v_add_f32_e32 v27, v27, v235
	s_waitcnt vmcnt(25)
	v_add_f32_e32 v27, v27, v236
	s_waitcnt vmcnt(24)
	v_add_f32_e32 v27, v27, v237
	s_waitcnt vmcnt(23)
	v_add_f32_e32 v27, v27, v238
	s_waitcnt vmcnt(22)
	v_add_f32_e32 v27, v27, v239
	s_waitcnt vmcnt(21)
	v_add_f32_e32 v27, v27, v240
	s_waitcnt vmcnt(20)
	v_add_f32_e32 v27, v27, v241
	s_waitcnt vmcnt(19)
	v_add_f32_e32 v27, v27, v242
	s_waitcnt vmcnt(18)
	v_add_f32_e32 v27, v27, v243
	s_waitcnt vmcnt(17)
	v_add_f32_e32 v27, v27, v244
	s_waitcnt vmcnt(16)
	v_add_f32_e32 v27, v27, v245
	s_waitcnt vmcnt(15)
	v_add_f32_e32 v27, v27, v248
	s_waitcnt vmcnt(14)
	v_add_f32_e32 v27, v27, v249
	s_waitcnt vmcnt(13)
	v_add_f32_e32 v27, v27, v250
	s_waitcnt vmcnt(12)
	v_add_f32_e32 v27, v27, v251
	s_waitcnt vmcnt(11)
	v_add_f32_e32 v27, v27, v252
	s_waitcnt vmcnt(10)
	v_add_f32_e32 v27, v27, v253
	s_waitcnt vmcnt(9)
	v_add_f32_e32 v27, v27, v254
	s_waitcnt vmcnt(8)
	v_add_f32_e32 v27, v27, v255
	s_waitcnt vmcnt(7)
	v_add_f32_e32 v27, v27, v200
	s_waitcnt vmcnt(6)
	v_add_f32_e32 v27, v27, v201
	s_waitcnt vmcnt(5)
	v_add_f32_e32 v27, v27, v202
	s_waitcnt vmcnt(4)
	v_add_f32_e32 v27, v27, v204
	s_waitcnt vmcnt(3)
	v_add_f32_e32 v27, v27, v205
	s_waitcnt vmcnt(2)
	v_add_f32_e32 v27, v27, v109
	s_waitcnt vmcnt(1)
	v_add_f32_e32 v27, v27, v119
	s_waitcnt vmcnt(0)
	v_add_f32_e32 v27, v27, v189
	s_waitcnt lgkmcnt(4)
	v_add_f32_e32 v8, 0, v8
	v_add_f32_e32 v8, v8, v9
	s_waitcnt lgkmcnt(3)
	v_add_f32_e32 v6, v8, v6
	v_add_f32_e32 v6, v6, v7
	s_waitcnt lgkmcnt(2)
	v_add_f32_e32 v4, v6, v4
	v_add_f32_e32 v4, v4, v5
	s_waitcnt lgkmcnt(1)
	v_add_f32_e32 v2, v4, v2
	v_add_f32_e32 v2, v2, v3
	v_fmac_f32_e32 v27, v10, v2
	ds_write_b32 v98, v27 offset:51200
	s_and_saveexec_b64 s[6:7], s[4:5]
	ds_write_b32 v92, v10 offset:55424
	s_or_b64 exec, exec, s[6:7]
	v_mov_b32_e32 v4, 0
	v_mov_b32_e32 v12, 0
	v_mov_b32_e32 v11, 0
	v_mov_b32_e32 v10, 0
	v_mov_b32_e32 v9, 0
	v_mov_b32_e32 v5, 0
	v_mov_b32_e32 v2, 0
	v_mov_b32_e32 v3, 0
	v_mov_b32_e32 v6, 0
	v_mov_b32_e32 v7, 0
	v_mov_b32_e32 v22, 0
	v_mov_b32_e32 v8, 0
	s_waitcnt lgkmcnt(0)
	s_barrier
	s_and_saveexec_b64 s[6:7], s[4:5]
	s_cbranch_execz .LBB0_904
	v_add_u32_e32 v4, 0xc800, v100
	ds_read2_b32 v[2:3], v4 offset1:1
	v_add_u32_e32 v5, 0xc808, v100
	v_add_u32_e32 v8, 0xc810, v100
	v_add_u32_e32 v9, 0xc818, v100
	ds_read2_b32 v[6:7], v5 offset1:1
	ds_read2_b32 v[10:11], v8 offset1:1
	ds_read2_b32 v[12:13], v9 offset1:1
	s_waitcnt lgkmcnt(3)
	v_max_f32_e32 v2, v2, v2
	v_max_f32_e32 v2, 0xff800000, v2
	v_cmp_gt_f32_e32 vcc, v3, v2
	s_nop 1
	v_cndmask_b32_e32 v2, v2, v3, vcc
	v_cndmask_b32_e64 v14, 0, 1, vcc
	s_waitcnt lgkmcnt(2)
	v_cmp_gt_f32_e32 vcc, v6, v2
	s_nop 1
	v_cndmask_b32_e32 v2, v2, v6, vcc
	v_cndmask_b32_e64 v3, v14, 2, vcc
	v_cmp_gt_f32_e32 vcc, v7, v2
	s_nop 1
	v_cndmask_b32_e32 v2, v2, v7, vcc
	v_cndmask_b32_e64 v3, v3, 3, vcc
	s_waitcnt lgkmcnt(1)
	v_cmp_gt_f32_e32 vcc, v10, v2
	s_nop 1
	v_cndmask_b32_e32 v2, v2, v10, vcc
	v_cndmask_b32_e64 v3, v3, 4, vcc
	v_cmp_gt_f32_e32 vcc, v11, v2
	v_add_u32_e32 v10, 0xc820, v100
	s_nop 0
	v_cndmask_b32_e32 v2, v2, v11, vcc
	v_cndmask_b32_e64 v3, v3, 5, vcc
	s_waitcnt lgkmcnt(0)
	v_cmp_gt_f32_e32 vcc, v12, v2
	v_add_u32_e32 v11, 0xc828, v100
	s_nop 0
	v_cndmask_b32_e32 v2, v2, v12, vcc
	v_cndmask_b32_e64 v3, v3, 6, vcc
	v_cmp_gt_f32_e32 vcc, v13, v2
	v_add_u32_e32 v12, 0xc830, v100
	s_nop 0
	v_cndmask_b32_e64 v18, v3, 7, vcc
	v_cndmask_b32_e32 v19, v2, v13, vcc
	ds_read2_b32 v[2:3], v10 offset1:1
	v_add_u32_e32 v13, 0xc838, v100
	ds_read2_b32 v[6:7], v11 offset1:1
	ds_read2_b32 v[14:15], v12 offset1:1
	ds_read2_b32 v[16:17], v13 offset1:1
	s_waitcnt lgkmcnt(3)
; __device__ __forceinline__ void p7_router(Frame& F, const Args& A, bool commit = true) {
;     ...
;             for (int k = 0; k < 4; ++k) { float best = -INFINITY; int bi = 0;
;                 for (int e = 0; e < 32; ++e) { const float v = logitL[F.tid * 33 + e]; if (v > best) { best = v; bi = e; } }
;                 sv[k] = best; se[k] = bi; logitL[F.tid * 33 + bi] = -INFINITY; }
	v_cmp_gt_f32_e32 vcc, v2, v19
	s_nop 1
	v_cndmask_b32_e32 v2, v19, v2, vcc
	v_cndmask_b32_e64 v18, v18, 8, vcc
	v_cmp_gt_f32_e32 vcc, v3, v2
	s_nop 1
	v_cndmask_b32_e32 v2, v2, v3, vcc
	v_cndmask_b32_e64 v18, v18, 9, vcc
	s_waitcnt lgkmcnt(2)
	v_cmp_gt_f32_e32 vcc, v6, v2
	s_nop 1
	v_cndmask_b32_e32 v2, v2, v6, vcc
	v_cndmask_b32_e64 v3, v18, 10, vcc
	v_cmp_gt_f32_e32 vcc, v7, v2
	s_nop 1
	v_cndmask_b32_e32 v2, v2, v7, vcc
	v_cndmask_b32_e64 v3, v3, 11, vcc
	s_waitcnt lgkmcnt(1)
	v_cmp_gt_f32_e32 vcc, v14, v2
	s_nop 1
	v_cndmask_b32_e32 v2, v2, v14, vcc
	v_cndmask_b32_e64 v3, v3, 12, vcc
	v_cmp_gt_f32_e32 vcc, v15, v2
	v_add_u32_e32 v14, 0xc840, v100
	s_nop 0
	v_cndmask_b32_e32 v2, v2, v15, vcc
	v_cndmask_b32_e64 v3, v3, 13, vcc
	s_waitcnt lgkmcnt(0)
	v_cmp_gt_f32_e32 vcc, v16, v2
	v_add_u32_e32 v15, 0xc848, v100
	s_nop 0
	v_cndmask_b32_e32 v2, v2, v16, vcc
	v_cndmask_b32_e64 v3, v3, 14, vcc
	v_cmp_gt_f32_e32 vcc, v17, v2
	v_add_u32_e32 v16, 0xc850, v100
	s_nop 0
	v_cndmask_b32_e64 v22, v3, 15, vcc
	v_cndmask_b32_e32 v23, v2, v17, vcc
	ds_read2_b32 v[2:3], v14 offset1:1
	v_add_u32_e32 v17, 0xc858, v100
	ds_read2_b32 v[6:7], v15 offset1:1
	ds_read2_b32 v[18:19], v16 offset1:1
	ds_read2_b32 v[20:21], v17 offset1:1
	s_waitcnt lgkmcnt(3)
	v_cmp_gt_f32_e32 vcc, v2, v23
	s_nop 1
	v_cndmask_b32_e32 v2, v23, v2, vcc
	v_cndmask_b32_e64 v22, v22, 16, vcc
	v_cmp_gt_f32_e32 vcc, v3, v2
	s_nop 1
	v_cndmask_b32_e32 v2, v2, v3, vcc
	v_cndmask_b32_e64 v22, v22, 17, vcc
	s_waitcnt lgkmcnt(2)
	v_cmp_gt_f32_e32 vcc, v6, v2
	s_nop 1
	v_cndmask_b32_e32 v2, v2, v6, vcc
	v_cndmask_b32_e64 v3, v22, 18, vcc
	v_cmp_gt_f32_e32 vcc, v7, v2
	s_nop 1
	v_cndmask_b32_e32 v2, v2, v7, vcc
	v_cndmask_b32_e64 v3, v3, 19, vcc
	s_waitcnt lgkmcnt(1)
	v_cmp_gt_f32_e32 vcc, v18, v2
	s_nop 1
	v_cndmask_b32_e32 v2, v2, v18, vcc
	v_cndmask_b32_e64 v3, v3, 20, vcc
	v_cmp_gt_f32_e32 vcc, v19, v2
	v_add_u32_e32 v18, 0xc860, v100
	s_nop 0
	v_cndmask_b32_e32 v2, v2, v19, vcc
	v_cndmask_b32_e64 v3, v3, 21, vcc
	s_waitcnt lgkmcnt(0)
	v_cmp_gt_f32_e32 vcc, v20, v2
	v_add_u32_e32 v19, 0xc868, v100
	s_nop 0
	v_cndmask_b32_e32 v2, v2, v20, vcc
	v_cndmask_b32_e64 v3, v3, 22, vcc
	v_cmp_gt_f32_e32 vcc, v21, v2
	v_add_u32_e32 v20, 0xc870, v100
	s_nop 0
	v_cndmask_b32_e64 v26, v3, 23, vcc
	v_cndmask_b32_e32 v27, v2, v21, vcc
	ds_read2_b32 v[2:3], v18 offset1:1
	v_add_u32_e32 v21, 0xc878, v100
	ds_read2_b32 v[6:7], v19 offset1:1
	ds_read2_b32 v[22:23], v20 offset1:1
	ds_read2_b32 v[24:25], v21 offset1:1
	s_waitcnt lgkmcnt(3)
	v_cmp_gt_f32_e32 vcc, v2, v27
	s_nop 1
	v_cndmask_b32_e32 v2, v27, v2, vcc
	v_cndmask_b32_e64 v26, v26, 24, vcc
	v_cmp_gt_f32_e32 vcc, v3, v2
	s_nop 1
	v_cndmask_b32_e32 v2, v2, v3, vcc
	v_cndmask_b32_e64 v26, v26, 25, vcc
	s_waitcnt lgkmcnt(2)
	v_cmp_gt_f32_e32 vcc, v6, v2
	s_nop 1
	v_cndmask_b32_e32 v2, v2, v6, vcc
	v_cndmask_b32_e64 v3, v26, 26, vcc
	v_cmp_gt_f32_e32 vcc, v7, v2
	s_nop 1
	v_cndmask_b32_e32 v2, v2, v7, vcc
	v_cndmask_b32_e64 v3, v3, 27, vcc
	s_waitcnt lgkmcnt(1)
	v_cmp_gt_f32_e32 vcc, v22, v2
	s_nop 1
	v_cndmask_b32_e32 v2, v2, v22, vcc
	v_cndmask_b32_e64 v3, v3, 28, vcc
	v_cmp_gt_f32_e32 vcc, v23, v2
	s_nop 1
	v_cndmask_b32_e32 v2, v2, v23, vcc
	v_cndmask_b32_e64 v3, v3, 29, vcc
	s_waitcnt lgkmcnt(0)
	v_cmp_gt_f32_e32 vcc, v24, v2
	s_nop 1
	v_cndmask_b32_e32 v7, v2, v24, vcc
	v_cndmask_b32_e64 v3, v3, 30, vcc
	v_cmp_gt_f32_e32 vcc, v25, v7
	s_nop 1
	v_cndmask_b32_e64 v6, v3, 31, vcc
	v_lshlrev_b32_e32 v2, 2, v6
	v_add_u32_e32 v3, v100, v2
	ds_write_b32 v3, v106 offset:51200
	ds_read2_b32 v[22:23], v4 offset1:1
	v_cndmask_b32_e32 v3, v7, v25, vcc
	ds_read2_b32 v[24:25], v5 offset1:1
	ds_read2_b32 v[26:27], v8 offset1:1
	ds_read2_b32 v[28:29], v9 offset1:1
	v_add_u32_e32 v2, 0, v2
	s_waitcnt lgkmcnt(3)
	v_max_f32_e32 v7, v22, v22
	v_max_f32_e32 v7, 0xff800000, v7
	v_cmp_gt_f32_e32 vcc, v23, v7
	s_nop 1
	v_cndmask_b32_e32 v7, v7, v23, vcc
	v_cndmask_b32_e64 v22, 0, 1, vcc
	s_waitcnt lgkmcnt(2)
	v_cmp_gt_f32_e32 vcc, v24, v7
	s_nop 1
	v_cndmask_b32_e32 v7, v7, v24, vcc
	v_cndmask_b32_e64 v22, v22, 2, vcc
	v_cmp_gt_f32_e32 vcc, v25, v7
	s_nop 1
	v_cndmask_b32_e32 v7, v7, v25, vcc
	v_cndmask_b32_e64 v22, v22, 3, vcc
	s_waitcnt lgkmcnt(1)
	v_cmp_gt_f32_e32 vcc, v26, v7
	s_nop 1
	v_cndmask_b32_e32 v7, v7, v26, vcc
	v_cndmask_b32_e64 v22, v22, 4, vcc
	v_cmp_gt_f32_e32 vcc, v27, v7
	s_nop 1
	v_cndmask_b32_e32 v7, v7, v27, vcc
	v_cndmask_b32_e64 v22, v22, 5, vcc
	s_waitcnt lgkmcnt(0)
	v_cmp_gt_f32_e32 vcc, v28, v7
	s_nop 1
	v_cndmask_b32_e32 v7, v7, v28, vcc
	v_cndmask_b32_e64 v22, v22, 6, vcc
	v_cmp_gt_f32_e32 vcc, v29, v7
	s_nop 1
	v_cndmask_b32_e64 v30, v22, 7, vcc
	ds_read2_b32 v[22:23], v10 offset1:1
	v_cndmask_b32_e32 v7, v7, v29, vcc
	ds_read2_b32 v[24:25], v11 offset1:1
	ds_read2_b32 v[26:27], v12 offset1:1
	ds_read2_b32 v[28:29], v13 offset1:1
	s_waitcnt lgkmcnt(3)
	v_cmp_gt_f32_e32 vcc, v22, v7
	s_nop 1
	v_cndmask_b32_e32 v7, v7, v22, vcc
	v_cndmask_b32_e64 v30, v30, 8, vcc
	v_cmp_gt_f32_e32 vcc, v23, v7
	s_nop 1
	v_cndmask_b32_e32 v7, v7, v23, vcc
	v_cndmask_b32_e64 v22, v30, 9, vcc
	s_waitcnt lgkmcnt(2)
	v_cmp_gt_f32_e32 vcc, v24, v7
	s_nop 1
	v_cndmask_b32_e32 v7, v7, v24, vcc
	v_cndmask_b32_e64 v22, v22, 10, vcc
	v_cmp_gt_f32_e32 vcc, v25, v7
	s_nop 1
	v_cndmask_b32_e32 v7, v7, v25, vcc
	v_cndmask_b32_e64 v22, v22, 11, vcc
	s_waitcnt lgkmcnt(1)
	v_cmp_gt_f32_e32 vcc, v26, v7
	s_nop 1
	v_cndmask_b32_e32 v7, v7, v26, vcc
	v_cndmask_b32_e64 v22, v22, 12, vcc
	v_cmp_gt_f32_e32 vcc, v27, v7
	s_nop 1
	v_cndmask_b32_e32 v7, v7, v27, vcc
	v_cndmask_b32_e64 v22, v22, 13, vcc
	s_waitcnt lgkmcnt(0)
; __device__ __forceinline__ void p7_router(Frame& F, const Args& A, bool commit = true) {
;     ...
;             for (int k = 0; k < 4; ++k) { float best = -INFINITY; int bi = 0;
;                 for (int e = 0; e < 32; ++e) { const float v = logitL[F.tid * 33 + e]; if (v > best) { best = v; bi = e; } }
;                 sv[k] = best; se[k] = bi; logitL[F.tid * 33 + bi] = -INFINITY; }
	v_cmp_gt_f32_e32 vcc, v28, v7
	s_nop 1
	v_cndmask_b32_e32 v7, v7, v28, vcc
	v_cndmask_b32_e64 v22, v22, 14, vcc
	v_cmp_gt_f32_e32 vcc, v29, v7
	s_nop 1
	v_cndmask_b32_e64 v30, v22, 15, vcc
	ds_read2_b32 v[22:23], v14 offset1:1
	v_cndmask_b32_e32 v7, v7, v29, vcc
	ds_read2_b32 v[24:25], v15 offset1:1
	ds_read2_b32 v[26:27], v16 offset1:1
	ds_read2_b32 v[28:29], v17 offset1:1
	s_waitcnt lgkmcnt(3)
	v_cmp_gt_f32_e32 vcc, v22, v7
	s_nop 1
	v_cndmask_b32_e32 v7, v7, v22, vcc
	v_cndmask_b32_e64 v30, v30, 16, vcc
	v_cmp_gt_f32_e32 vcc, v23, v7
	s_nop 1
	v_cndmask_b32_e32 v7, v7, v23, vcc
	v_cndmask_b32_e64 v22, v30, 17, vcc
	s_waitcnt lgkmcnt(2)
	v_cmp_gt_f32_e32 vcc, v24, v7
	s_nop 1
	v_cndmask_b32_e32 v7, v7, v24, vcc
	v_cndmask_b32_e64 v22, v22, 18, vcc
	v_cmp_gt_f32_e32 vcc, v25, v7
	s_nop 1
	v_cndmask_b32_e32 v7, v7, v25, vcc
	v_cndmask_b32_e64 v22, v22, 19, vcc
	s_waitcnt lgkmcnt(1)
	v_cmp_gt_f32_e32 vcc, v26, v7
	s_nop 1
	v_cndmask_b32_e32 v7, v7, v26, vcc
	v_cndmask_b32_e64 v22, v22, 20, vcc
	v_cmp_gt_f32_e32 vcc, v27, v7
	s_nop 1
	v_cndmask_b32_e32 v7, v7, v27, vcc
	v_cndmask_b32_e64 v22, v22, 21, vcc
	s_waitcnt lgkmcnt(0)
	v_cmp_gt_f32_e32 vcc, v28, v7
	s_nop 1
	v_cndmask_b32_e32 v7, v7, v28, vcc
	v_cndmask_b32_e64 v22, v22, 22, vcc
	v_cmp_gt_f32_e32 vcc, v29, v7
	s_nop 1
	v_cndmask_b32_e64 v30, v22, 23, vcc
	ds_read2_b32 v[22:23], v18 offset1:1
	v_cndmask_b32_e32 v7, v7, v29, vcc
	ds_read2_b32 v[24:25], v19 offset1:1
	ds_read2_b32 v[26:27], v20 offset1:1
	ds_read2_b32 v[28:29], v21 offset1:1
	s_waitcnt lgkmcnt(3)
	v_cmp_gt_f32_e32 vcc, v22, v7
	s_nop 1
	v_cndmask_b32_e32 v7, v7, v22, vcc
	v_cndmask_b32_e64 v30, v30, 24, vcc
	v_cmp_gt_f32_e32 vcc, v23, v7
	s_nop 1
	v_cndmask_b32_e32 v7, v7, v23, vcc
	v_cndmask_b32_e64 v22, v30, 25, vcc
	s_waitcnt lgkmcnt(2)
	v_cmp_gt_f32_e32 vcc, v24, v7
	s_nop 1
	v_cndmask_b32_e32 v7, v7, v24, vcc
	v_cndmask_b32_e64 v22, v22, 26, vcc
	v_cmp_gt_f32_e32 vcc, v25, v7
	s_nop 1
	v_cndmask_b32_e32 v7, v7, v25, vcc
	v_cndmask_b32_e64 v22, v22, 27, vcc
	s_waitcnt lgkmcnt(1)
	v_cmp_gt_f32_e32 vcc, v26, v7
	s_nop 1
	v_cndmask_b32_e32 v7, v7, v26, vcc
	v_cndmask_b32_e64 v22, v22, 28, vcc
	v_cmp_gt_f32_e32 vcc, v27, v7
	s_nop 1
	v_cndmask_b32_e32 v7, v7, v27, vcc
	v_cndmask_b32_e64 v22, v22, 29, vcc
	s_waitcnt lgkmcnt(0)
	v_cmp_gt_f32_e32 vcc, v28, v7
	s_nop 1
	v_cndmask_b32_e32 v24, v7, v28, vcc
	v_cndmask_b32_e64 v22, v22, 30, vcc
	v_cmp_gt_f32_e32 vcc, v29, v24
	s_nop 1
	v_cndmask_b32_e64 v7, v22, 31, vcc
	v_lshlrev_b32_e32 v30, 2, v7
	v_add_u32_e32 v22, v100, v30
	ds_write_b32 v22, v106 offset:51200
	ds_read2_b32 v[22:23], v4 offset1:1
	v_cndmask_b32_e32 v31, v24, v29, vcc
	ds_read2_b32 v[24:25], v5 offset1:1
	ds_read2_b32 v[26:27], v8 offset1:1
	ds_read2_b32 v[28:29], v9 offset1:1
	s_waitcnt lgkmcnt(3)
	v_max_f32_e32 v22, v22, v22
	v_max_f32_e32 v22, 0xff800000, v22
	v_cmp_gt_f32_e32 vcc, v23, v22
	s_nop 1
	v_cndmask_b32_e32 v22, v22, v23, vcc
	v_cndmask_b32_e64 v32, 0, 1, vcc
	s_waitcnt lgkmcnt(2)
	v_cmp_gt_f32_e32 vcc, v24, v22
	s_nop 1
	v_cndmask_b32_e32 v22, v22, v24, vcc
	v_cndmask_b32_e64 v23, v32, 2, vcc
	v_cmp_gt_f32_e32 vcc, v25, v22
	s_nop 1
	v_cndmask_b32_e32 v22, v22, v25, vcc
	v_cndmask_b32_e64 v23, v23, 3, vcc
	s_waitcnt lgkmcnt(1)
	v_cmp_gt_f32_e32 vcc, v26, v22
	s_nop 1
	v_cndmask_b32_e32 v22, v22, v26, vcc
	v_cndmask_b32_e64 v23, v23, 4, vcc
	v_cmp_gt_f32_e32 vcc, v27, v22
	s_nop 1
	v_cndmask_b32_e32 v22, v22, v27, vcc
	v_cndmask_b32_e64 v23, v23, 5, vcc
	s_waitcnt lgkmcnt(0)
	v_cmp_gt_f32_e32 vcc, v28, v22
	s_nop 1
	v_cndmask_b32_e32 v24, v22, v28, vcc
	v_cndmask_b32_e64 v23, v23, 6, vcc
	v_cmp_gt_f32_e32 vcc, v29, v24
	s_nop 1
	v_cndmask_b32_e64 v32, v23, 7, vcc
	ds_read2_b32 v[22:23], v10 offset1:1
	v_cndmask_b32_e32 v33, v24, v29, vcc
	ds_read2_b32 v[24:25], v11 offset1:1
	ds_read2_b32 v[26:27], v12 offset1:1
	ds_read2_b32 v[28:29], v13 offset1:1
	s_waitcnt lgkmcnt(3)
	v_cmp_gt_f32_e32 vcc, v22, v33
	s_nop 1
	v_cndmask_b32_e32 v22, v33, v22, vcc
	v_cndmask_b32_e64 v32, v32, 8, vcc
	v_cmp_gt_f32_e32 vcc, v23, v22
	s_nop 1
	v_cndmask_b32_e32 v22, v22, v23, vcc
	v_cndmask_b32_e64 v32, v32, 9, vcc
	s_waitcnt lgkmcnt(2)
	v_cmp_gt_f32_e32 vcc, v24, v22
	s_nop 1
	v_cndmask_b32_e32 v22, v22, v24, vcc
	v_cndmask_b32_e64 v23, v32, 10, vcc
	v_cmp_gt_f32_e32 vcc, v25, v22
	s_nop 1
	v_cndmask_b32_e32 v22, v22, v25, vcc
	v_cndmask_b32_e64 v23, v23, 11, vcc
	s_waitcnt lgkmcnt(1)
	v_cmp_gt_f32_e32 vcc, v26, v22
	s_nop 1
	v_cndmask_b32_e32 v22, v22, v26, vcc
	v_cndmask_b32_e64 v23, v23, 12, vcc
	v_cmp_gt_f32_e32 vcc, v27, v22
	s_nop 1
	v_cndmask_b32_e32 v22, v22, v27, vcc
	v_cndmask_b32_e64 v23, v23, 13, vcc
	s_waitcnt lgkmcnt(0)
	v_cmp_gt_f32_e32 vcc, v28, v22
	s_nop 1
	v_cndmask_b32_e32 v24, v22, v28, vcc
	v_cndmask_b32_e64 v23, v23, 14, vcc
	v_cmp_gt_f32_e32 vcc, v29, v24
	s_nop 1
	v_cndmask_b32_e64 v32, v23, 15, vcc
	ds_read2_b32 v[22:23], v14 offset1:1
	v_cndmask_b32_e32 v33, v24, v29, vcc
	ds_read2_b32 v[24:25], v15 offset1:1
	ds_read2_b32 v[26:27], v16 offset1:1
	ds_read2_b32 v[28:29], v17 offset1:1
	s_waitcnt lgkmcnt(3)
	v_cmp_gt_f32_e32 vcc, v22, v33
	s_nop 1
	v_cndmask_b32_e32 v22, v33, v22, vcc
	v_cndmask_b32_e64 v32, v32, 16, vcc
	v_cmp_gt_f32_e32 vcc, v23, v22
	s_nop 1
	v_cndmask_b32_e32 v22, v22, v23, vcc
	v_cndmask_b32_e64 v32, v32, 17, vcc
	s_waitcnt lgkmcnt(2)
	v_cmp_gt_f32_e32 vcc, v24, v22
	s_nop 1
	v_cndmask_b32_e32 v22, v22, v24, vcc
	v_cndmask_b32_e64 v23, v32, 18, vcc
	v_cmp_gt_f32_e32 vcc, v25, v22
	s_nop 1
	v_cndmask_b32_e32 v22, v22, v25, vcc
	v_cndmask_b32_e64 v23, v23, 19, vcc
	s_waitcnt lgkmcnt(1)
; __device__ __forceinline__ void p7_router(Frame& F, const Args& A, bool commit = true) {
;     ...
;             for (int k = 0; k < 4; ++k) { float best = -INFINITY; int bi = 0;
;                 for (int e = 0; e < 32; ++e) { const float v = logitL[F.tid * 33 + e]; if (v > best) { best = v; bi = e; } }
;                 sv[k] = best; se[k] = bi; logitL[F.tid * 33 + bi] = -INFINITY; }
	v_cmp_gt_f32_e32 vcc, v26, v22
	s_nop 1
	v_cndmask_b32_e32 v22, v22, v26, vcc
	v_cndmask_b32_e64 v23, v23, 20, vcc
	v_cmp_gt_f32_e32 vcc, v27, v22
	s_nop 1
	v_cndmask_b32_e32 v22, v22, v27, vcc
	v_cndmask_b32_e64 v23, v23, 21, vcc
	s_waitcnt lgkmcnt(0)
	v_cmp_gt_f32_e32 vcc, v28, v22
	s_nop 1
	v_cndmask_b32_e32 v24, v22, v28, vcc
	v_cndmask_b32_e64 v23, v23, 22, vcc
	v_cmp_gt_f32_e32 vcc, v29, v24
	s_nop 1
	v_cndmask_b32_e64 v32, v23, 23, vcc
	ds_read2_b32 v[22:23], v18 offset1:1
	v_cndmask_b32_e32 v33, v24, v29, vcc
	ds_read2_b32 v[24:25], v19 offset1:1
	ds_read2_b32 v[26:27], v20 offset1:1
	ds_read2_b32 v[28:29], v21 offset1:1
	s_waitcnt lgkmcnt(3)
	v_cmp_gt_f32_e32 vcc, v22, v33
	s_nop 1
	v_cndmask_b32_e32 v22, v33, v22, vcc
	v_cndmask_b32_e64 v32, v32, 24, vcc
	v_cmp_gt_f32_e32 vcc, v23, v22
	s_nop 1
	v_cndmask_b32_e32 v22, v22, v23, vcc
	v_cndmask_b32_e64 v32, v32, 25, vcc
	s_waitcnt lgkmcnt(2)
	v_cmp_gt_f32_e32 vcc, v24, v22
	s_nop 1
	v_cndmask_b32_e32 v22, v22, v24, vcc
	v_cndmask_b32_e64 v23, v32, 26, vcc
	v_cmp_gt_f32_e32 vcc, v25, v22
	s_nop 1
	v_cndmask_b32_e32 v22, v22, v25, vcc
	v_cndmask_b32_e64 v23, v23, 27, vcc
	s_waitcnt lgkmcnt(1)
	v_cmp_gt_f32_e32 vcc, v26, v22
	s_nop 1
	v_cndmask_b32_e32 v22, v22, v26, vcc
	v_cndmask_b32_e64 v23, v23, 28, vcc
	v_cmp_gt_f32_e32 vcc, v27, v22
	s_nop 1
	v_cndmask_b32_e32 v22, v22, v27, vcc
	v_cndmask_b32_e64 v23, v23, 29, vcc
	s_waitcnt lgkmcnt(0)
	v_cmp_gt_f32_e32 vcc, v28, v22
	s_nop 1
	v_cndmask_b32_e32 v26, v22, v28, vcc
	v_cndmask_b32_e64 v23, v23, 30, vcc
	v_cmp_gt_f32_e32 vcc, v29, v26
	s_nop 1
	v_cndmask_b32_e64 v22, v23, 31, vcc
	v_lshlrev_b32_e32 v23, 2, v22
	v_add_u32_e32 v24, v100, v23
	ds_write_b32 v24, v106 offset:51200
	ds_read2_b32 v[24:25], v4 offset1:1
	v_cndmask_b32_e32 v28, v26, v29, vcc
	ds_read2_b32 v[4:5], v5 offset1:1
	ds_read2_b32 v[26:27], v8 offset1:1
	ds_read2_b32 v[8:9], v9 offset1:1
	s_waitcnt lgkmcnt(3)
	v_max_f32_e32 v24, v24, v24
	v_max_f32_e32 v24, 0xff800000, v24
	v_cmp_gt_f32_e32 vcc, v25, v24
	s_nop 1
	v_cndmask_b32_e32 v24, v24, v25, vcc
	v_cndmask_b32_e64 v29, 0, 1, vcc
	s_waitcnt lgkmcnt(2)
	v_cmp_gt_f32_e32 vcc, v4, v24
	s_nop 1
	v_cndmask_b32_e32 v4, v24, v4, vcc
	v_cndmask_b32_e64 v25, v29, 2, vcc
	v_cmp_gt_f32_e32 vcc, v5, v4
	s_nop 1
	v_cndmask_b32_e32 v4, v4, v5, vcc
	v_cndmask_b32_e64 v24, v25, 3, vcc
	s_waitcnt lgkmcnt(1)
	v_cmp_gt_f32_e32 vcc, v26, v4
	s_nop 1
	v_cndmask_b32_e32 v4, v4, v26, vcc
	v_cndmask_b32_e64 v5, v24, 4, vcc
	v_cmp_gt_f32_e32 vcc, v27, v4
	s_nop 1
	v_cndmask_b32_e32 v4, v4, v27, vcc
	v_cndmask_b32_e64 v5, v5, 5, vcc
	s_waitcnt lgkmcnt(0)
	v_cmp_gt_f32_e32 vcc, v8, v4
	s_nop 1
	v_cndmask_b32_e32 v8, v4, v8, vcc
	v_cndmask_b32_e64 v5, v5, 6, vcc
	v_cmp_gt_f32_e32 vcc, v9, v8
	s_nop 1
	v_cndmask_b32_e64 v24, v5, 7, vcc
	ds_read2_b32 v[4:5], v10 offset1:1
	v_cndmask_b32_e32 v25, v8, v9, vcc
	ds_read2_b32 v[8:9], v11 offset1:1
	ds_read2_b32 v[10:11], v12 offset1:1
	ds_read2_b32 v[12:13], v13 offset1:1
	s_waitcnt lgkmcnt(3)
	v_cmp_gt_f32_e32 vcc, v4, v25
	s_nop 1
	v_cndmask_b32_e32 v4, v25, v4, vcc
	v_cndmask_b32_e64 v24, v24, 8, vcc
	v_cmp_gt_f32_e32 vcc, v5, v4
	s_nop 1
	v_cndmask_b32_e32 v4, v4, v5, vcc
	v_cndmask_b32_e64 v24, v24, 9, vcc
	s_waitcnt lgkmcnt(2)
	v_cmp_gt_f32_e32 vcc, v8, v4
	s_nop 1
	v_cndmask_b32_e32 v4, v4, v8, vcc
	v_cndmask_b32_e64 v5, v24, 10, vcc
	v_cmp_gt_f32_e32 vcc, v9, v4
	s_nop 1
	v_cndmask_b32_e32 v4, v4, v9, vcc
	v_cndmask_b32_e64 v5, v5, 11, vcc
	s_waitcnt lgkmcnt(1)
	v_cmp_gt_f32_e32 vcc, v10, v4
	s_nop 1
	v_cndmask_b32_e32 v4, v4, v10, vcc
	v_cndmask_b32_e64 v5, v5, 12, vcc
	v_cmp_gt_f32_e32 vcc, v11, v4
	s_nop 1
	v_cndmask_b32_e32 v4, v4, v11, vcc
	v_cndmask_b32_e64 v5, v5, 13, vcc
	s_waitcnt lgkmcnt(0)
	v_cmp_gt_f32_e32 vcc, v12, v4
	s_nop 1
	v_cndmask_b32_e32 v8, v4, v12, vcc
	v_cndmask_b32_e64 v5, v5, 14, vcc
	v_cmp_gt_f32_e32 vcc, v13, v8
	s_nop 1
	v_cndmask_b32_e64 v24, v5, 15, vcc
	ds_read2_b32 v[4:5], v14 offset1:1
	v_cndmask_b32_e32 v14, v8, v13, vcc
	ds_read2_b32 v[8:9], v15 offset1:1
	ds_read2_b32 v[10:11], v16 offset1:1
	ds_read2_b32 v[12:13], v17 offset1:1
	s_waitcnt lgkmcnt(3)
	v_cmp_gt_f32_e32 vcc, v4, v14
	s_nop 1
	v_cndmask_b32_e32 v4, v14, v4, vcc
	v_cndmask_b32_e64 v15, v24, 16, vcc
	v_cmp_gt_f32_e32 vcc, v5, v4
	s_nop 1
	v_cndmask_b32_e32 v4, v4, v5, vcc
	v_cndmask_b32_e64 v14, v15, 17, vcc
	s_waitcnt lgkmcnt(2)
; __device__ __forceinline__ void p7_router(Frame& F, const Args& A, bool commit = true) {
;     ...
;             for (int k = 0; k < 4; ++k) { float best = -INFINITY; int bi = 0;
;                 for (int e = 0; e < 32; ++e) { const float v = logitL[F.tid * 33 + e]; if (v > best) { best = v; bi = e; } }
;                 sv[k] = best; se[k] = bi; logitL[F.tid * 33 + bi] = -INFINITY; }
;             float sum = 0.f;
; #pragma unroll
;             for (int k = 0; k < 4; ++k) { pv[k] = expf(sv[k] - sv[0]); sum += pv[k]; }
;             const float inv = 1.0f / sum;
; #pragma unroll
;             for (int k = 0; k < 4; ++k) { pv[k] *= inv; lp[k] = __hip_atomic_fetch_add(lcnt + se[k], 1, __ATOMIC_RELAXED, __HIP_MEMORY_SCOPE_WORKGROUP); }
	v_cmp_gt_f32_e32 vcc, v8, v4
	s_nop 1
	v_cndmask_b32_e32 v4, v4, v8, vcc
	v_cndmask_b32_e64 v5, v14, 18, vcc
	v_cmp_gt_f32_e32 vcc, v9, v4
	s_nop 1
	v_cndmask_b32_e32 v4, v4, v9, vcc
	v_cndmask_b32_e64 v5, v5, 19, vcc
	s_waitcnt lgkmcnt(1)
	v_cmp_gt_f32_e32 vcc, v10, v4
	s_nop 1
	v_cndmask_b32_e32 v4, v4, v10, vcc
	v_cndmask_b32_e64 v5, v5, 20, vcc
	v_cmp_gt_f32_e32 vcc, v11, v4
	s_nop 1
	v_cndmask_b32_e32 v4, v4, v11, vcc
	v_cndmask_b32_e64 v5, v5, 21, vcc
	s_waitcnt lgkmcnt(0)
	v_cmp_gt_f32_e32 vcc, v12, v4
	s_nop 1
	v_cndmask_b32_e32 v8, v4, v12, vcc
	v_cndmask_b32_e64 v5, v5, 22, vcc
	v_cmp_gt_f32_e32 vcc, v13, v8
	s_nop 1
	v_cndmask_b32_e64 v14, v5, 23, vcc
	ds_read2_b32 v[4:5], v18 offset1:1
	v_cndmask_b32_e32 v15, v8, v13, vcc
	ds_read2_b32 v[8:9], v19 offset1:1
	ds_read2_b32 v[10:11], v20 offset1:1
	ds_read2_b32 v[12:13], v21 offset1:1
	s_waitcnt lgkmcnt(3)
	v_cmp_gt_f32_e32 vcc, v4, v15
	s_nop 1
	v_cndmask_b32_e32 v4, v15, v4, vcc
	v_cndmask_b32_e64 v14, v14, 24, vcc
	v_cmp_gt_f32_e32 vcc, v5, v4
	s_nop 1
	v_cndmask_b32_e32 v4, v4, v5, vcc
	v_cndmask_b32_e64 v14, v14, 25, vcc
	s_waitcnt lgkmcnt(2)
	v_cmp_gt_f32_e32 vcc, v8, v4
	s_nop 1
	v_cndmask_b32_e32 v4, v4, v8, vcc
	v_cndmask_b32_e64 v5, v14, 26, vcc
	v_cmp_gt_f32_e32 vcc, v9, v4
	s_nop 1
	v_cndmask_b32_e32 v4, v4, v9, vcc
	v_cndmask_b32_e64 v5, v5, 27, vcc
	s_waitcnt lgkmcnt(1)
	v_cmp_gt_f32_e32 vcc, v10, v4
	v_sub_f32_e32 v9, v3, v3
	v_mul_f32_e32 v8, 0x3fb8aa3b, v9
	v_cndmask_b32_e32 v4, v4, v10, vcc
	v_cndmask_b32_e64 v5, v5, 28, vcc
	v_cmp_gt_f32_e32 vcc, v11, v4
	v_fma_f32 v10, v9, s35, -v8
	v_fmac_f32_e32 v10, 0x32a5705f, v9
	v_cndmask_b32_e32 v4, v4, v11, vcc
	v_rndne_f32_e32 v11, v8
	v_sub_f32_e32 v8, v8, v11
	v_add_f32_e32 v8, v8, v10
	v_cndmask_b32_e64 v5, v5, 29, vcc
	s_waitcnt lgkmcnt(0)
	v_cmp_gt_f32_e32 vcc, v12, v4
	v_exp_f32_e32 v10, v8
	v_cvt_i32_f32_e32 v11, v11
	v_cndmask_b32_e32 v4, v4, v12, vcc
	v_cndmask_b32_e64 v5, v5, 30, vcc
	v_cmp_gt_f32_e32 vcc, v13, v4
	s_nop 1
	v_cndmask_b32_e64 v8, v5, 31, vcc
	v_sub_f32_e32 v5, v31, v3
	v_cndmask_b32_e32 v12, v4, v13, vcc
	v_ldexp_f32 v4, v10, v11
	v_mul_f32_e32 v10, 0x3fb8aa3b, v5
	v_fma_f32 v11, v5, s35, -v10
	v_rndne_f32_e32 v13, v10
	v_fmac_f32_e32 v11, 0x32a5705f, v5
	v_sub_f32_e32 v10, v10, v13
	v_add_f32_e32 v10, v10, v11
	v_exp_f32_e32 v10, v10
	v_cvt_i32_f32_e32 v11, v13
	v_cmp_ngt_f32_e32 vcc, s40, v9
	v_lshlrev_b32_e32 v16, 2, v8
	s_nop 0
	v_cndmask_b32_e32 v4, 0, v4, vcc
	v_cmp_nlt_f32_e32 vcc, s41, v9
	v_ldexp_f32 v9, v10, v11
	v_sub_f32_e32 v10, v28, v3
	v_mul_f32_e32 v11, 0x3fb8aa3b, v10
	v_fma_f32 v13, v10, s35, -v11
	v_rndne_f32_e32 v14, v11
	v_fmac_f32_e32 v13, 0x32a5705f, v10
	v_sub_f32_e32 v11, v11, v14
	v_add_f32_e32 v11, v11, v13
	v_exp_f32_e32 v11, v11
	v_cvt_i32_f32_e32 v13, v14
	v_sub_f32_e32 v3, v12, v3
	v_mul_f32_e32 v12, 0x3fb8aa3b, v3
	v_rndne_f32_e32 v14, v12
	v_ldexp_f32 v11, v11, v13
	v_fma_f32 v13, v3, s35, -v12
	v_fmac_f32_e32 v13, 0x32a5705f, v3
	v_sub_f32_e32 v12, v12, v14
	v_add_f32_e32 v12, v12, v13
	v_cndmask_b32_e32 v4, v108, v4, vcc
	v_cmp_ngt_f32_e32 vcc, s40, v5
	v_exp_f32_e32 v12, v12
	v_cvt_i32_f32_e32 v13, v14
	v_cndmask_b32_e32 v9, 0, v9, vcc
	v_cmp_nlt_f32_e32 vcc, s41, v5
	s_nop 1
	v_cndmask_b32_e32 v5, v108, v9, vcc
	v_cmp_ngt_f32_e32 vcc, s40, v10
	v_add_f32_e32 v9, v4, v5
	s_nop 0
	v_cndmask_b32_e32 v11, 0, v11, vcc
	v_cmp_nlt_f32_e32 vcc, s41, v10
	v_ldexp_f32 v10, v12, v13
	s_nop 0
	v_cndmask_b32_e32 v14, v108, v11, vcc
	v_cmp_ngt_f32_e32 vcc, s40, v3
	v_add_f32_e32 v9, v9, v14
	s_nop 0
	v_cndmask_b32_e32 v10, 0, v10, vcc
	v_cmp_nlt_f32_e32 vcc, s41, v3
	s_nop 1
	v_cndmask_b32_e32 v15, v108, v10, vcc
	v_add_f32_e32 v3, v9, v15
	v_div_scale_f32 v9, s[44:45], v3, v3, 1.0
	v_rcp_f32_e32 v13, v9
	v_add_u32_e32 v10, v100, v16
	ds_write_b32 v10, v106 offset:51200
	ds_add_rtn_u32 v12, v2, v107 offset:55552
	v_fma_f32 v10, -v9, v13, 1.0
	v_fmac_f32_e32 v13, v10, v13
	v_div_scale_f32 v10, vcc, 1.0, v3, 1.0
	v_mul_f32_e32 v17, v10, v13
	v_fma_f32 v11, -v9, v17, v10
	v_add_u32_e32 v2, 0, v30
	v_fmac_f32_e32 v17, v11, v13
	ds_add_rtn_u32 v11, v2, v107 offset:55552
	v_add_u32_e32 v2, 0, v23
	v_fma_f32 v18, -v9, v17, v10
	ds_add_rtn_u32 v10, v2, v107 offset:55552
	v_add_u32_e32 v2, 0, v16
	ds_add_rtn_u32 v9, v2, v107 offset:55552
	v_div_fmas_f32 v2, v18, v13, v17
	v_div_fixup_f32 v16, v2, v3, 1.0
	v_pk_mul_f32 v[2:3], v[14:15], v[16:17] op_sel_hi:[1,0]
	v_pk_mul_f32 v[4:5], v[4:5], v[16:17] op_sel_hi:[1,0]
